# expert gather phases: waves 4-7 start half a token period later (stagger) on top of v5
# speedup vs baseline: 1.0122x; 1.0122x over previous
.LBB0_1988:
	s_or_b64 exec, exec, s[6:7]
	s_mov_b64 s[6:7], s[0:1]
	s_waitcnt lgkmcnt(0)
	s_barrier
	v_readfirstlane_b32 s99, v0
	s_nop 3
	s_lshr_b32 s99, s99, 8
	s_cmp_eq_u32 s99, 0
	s_cbranch_scc1 .Lstag9_done
	s_sleep 56
.Lstag9_done:
	s_load_dwordx2 s[10:11], s[6:7], 0x90
	s_mov_b64 s[6:7], s[0:1]
	s_load_dwordx2 s[12:13], s[6:7], 0x90
	s_mov_b64 s[6:7], s[0:1]
	s_load_dwordx2 s[6:7], s[6:7], 0x90
	s_mov_b64 s[8:9], s[0:1]
	v_mov_b32_e32 v104, v0
	s_load_dwordx2 s[8:9], s[8:9], 0x90
	s_waitcnt lgkmcnt(0)
	s_add_u32 s6, s6, 0x40400000
	s_addc_u32 s7, s7, 0
	s_and_b32 s28, s2, -8
	v_ashrrev_i32_e32 v5, 6, v104
	v_add_u32_e32 v74, s28, v5
	v_ashrrev_i32_e32 v75, 31, v74
	v_and_b32_e32 v4, 63, v104
	v_mov_b32_e32 v87, 0
	v_lshlrev_b64 v[2:3], 8, v[74:75]
	v_lshl_add_u64 v[2:3], s[6:7], 0, v[2:3]
	v_lshlrev_b32_e32 v84, 2, v4
	v_mov_b32_e32 v85, v87
	v_lshl_add_u64 v[2:3], v[2:3], 0, v[84:85]
	global_load_dword v12, v[2:3], off
	s_lshl_b32 s27, s3, 22
	s_add_u32 s12, s12, s27
	v_and_b32_e32 v6, 15, v104
	v_lshrrev_b32_e32 v7, 2, v104
	s_addc_u32 s13, s13, 0
	s_lshl_b32 s26, s3, 9
	v_lshl_add_u32 v5, v5, 11, 0
	v_lshlrev_b32_e32 v86, 4, v6
	v_and_b32_e32 v98, 12, v7
	s_add_u32 s2, s10, s26
	s_mov_b64 s[14:15], 0xa300000
	v_lshl_add_u32 v113, v4, 3, v5
	v_add_u32_e32 v114, v5, v98
	v_lshl_add_u64 v[4:5], s[12:13], 0, v[86:87]
	s_addc_u32 s3, s11, 0
	s_mov_b64 s[16:17], 0x50c00000
	s_mov_b32 s18, 0x10000
	v_lshl_add_u64 v[76:77], v[4:5], 0, s[14:15]
	v_lshl_add_u64 v[4:5], s[2:3], 0, v[86:87]
	v_lshlrev_b64 v[6:7], 12, v[74:75]
	v_lshl_add_u64 v[78:79], v[4:5], 0, s[16:17]
	v_add_co_u32_e32 v2, vcc, s18, v2
	v_lshl_add_u64 v[10:11], v[78:79], 0, v[6:7]
	s_nop 0
	v_addc_co_u32_e32 v3, vcc, 0, v3, vcc
	global_load_dword v115, v[2:3], off
	global_load_dwordx4 v[6:9], v[10:11], off
	s_nop 0
	global_load_dwordx4 v[2:5], v[10:11], off offset:256
	s_add_u32 s2, s8, s27
	s_addc_u32 s3, s9, 0
	v_lshl_add_u64 v[102:103], s[2:3], 0, v[86:87]
	v_mov_b32_e32 v99, v87
	v_lshl_add_u64 v[86:87], v[102:103], 0, v[98:99]
	s_mov_b64 s[2:3], 0x1e400000
	v_and_b32_e32 v75, 8, v104
	v_cmp_lt_i32_e32 vcc, v160, v154
	v_lshl_add_u64 v[86:87], v[86:87], 0, s[2:3]
	v_cmp_eq_u32_e64 s[2:3], 0, v75
	v_cndmask_b32_e32 v75, v1, v160, vcc
	v_and_b32_e32 v98, 4, v104
	v_cmp_lt_i32_e32 vcc, v159, v154
	v_lshl_add_u64 v[84:85], s[6:7], 0, v[84:85]
	v_cmp_eq_u32_e64 s[6:7], 0, v98
	v_cndmask_b32_e32 v98, v1, v159, vcc
	v_lshlrev_b32_e32 v110, 2, v98
	v_and_b32_e32 v98, 2, v104
	v_cmp_lt_i32_e32 vcc, v158, v154
	v_cmp_eq_u32_e64 s[8:9], 0, v98
	s_mov_b32 s13, 0
	v_cndmask_b32_e32 v98, v1, v158, vcc
	v_lshlrev_b32_e32 v111, 2, v98
	v_and_b32_e32 v98, 1, v104
	v_cmp_lt_i32_e32 vcc, v157, v154
	v_cmp_eq_u32_e64 s[10:11], 0, v98
	v_add_u32_e32 v116, 0x200, v74
	v_cndmask_b32_e32 v98, v1, v157, vcc
	v_lshlrev_b32_e32 v75, 2, v75
	v_lshlrev_b32_e32 v112, 2, v98
	s_mov_b32 s16, 0xf0f0f0f0
	s_mov_b32 s17, 0
	s_waitcnt vmcnt(3)
	v_and_b32_e32 v10, 0xffff, v12
	v_lshrrev_b32_e32 v11, 16, v12
	ds_write_b64 v113, v[10:11]
	ds_read2_b32 v[10:11], v114 offset1:4
	ds_read2_b32 v[12:13], v114 offset0:8 offset1:12
	ds_read2_b32 v[14:15], v114 offset0:16 offset1:20
	ds_read2_b32 v[16:17], v114 offset0:24 offset1:28
	ds_read2_b32 v[42:43], v114 offset0:32 offset1:36
	s_waitcnt lgkmcnt(4)
	v_ashrrev_i32_e32 v19, 31, v10
	v_mov_b32_e32 v18, v10
	v_ashrrev_i32_e32 v21, 31, v11
	v_mov_b32_e32 v20, v11
	s_waitcnt lgkmcnt(3)
	v_ashrrev_i32_e32 v11, 31, v12
	v_mov_b32_e32 v10, v12
	v_ashrrev_i32_e32 v23, 31, v13
	v_mov_b32_e32 v22, v13
	s_waitcnt lgkmcnt(2)
	v_ashrrev_i32_e32 v13, 31, v14
	v_mov_b32_e32 v12, v14
	v_ashrrev_i32_e32 v25, 31, v15
	v_mov_b32_e32 v24, v15
	s_waitcnt lgkmcnt(1)
	v_ashrrev_i32_e32 v15, 31, v16
	v_mov_b32_e32 v14, v16
	v_ashrrev_i32_e32 v27, 31, v17
	v_mov_b32_e32 v26, v17
	v_lshlrev_b64 v[16:17], 8, v[18:19]
	v_lshlrev_b64 v[18:19], 8, v[20:21]
	v_lshlrev_b64 v[10:11], 8, v[10:11]
	v_lshlrev_b64 v[20:21], 8, v[22:23]
	v_lshlrev_b64 v[22:23], 8, v[24:25]
	v_lshlrev_b64 v[14:15], 8, v[14:15]
	v_lshlrev_b64 v[12:13], 8, v[12:13]
	v_lshlrev_b64 v[24:25], 8, v[26:27]
	v_lshl_add_u64 v[38:39], v[76:77], 0, v[16:17]
	v_lshl_add_u64 v[40:41], v[76:77], 0, v[18:19]
	v_lshl_add_u64 v[44:45], v[76:77], 0, v[10:11]
	v_lshl_add_u64 v[22:23], v[76:77], 0, v[22:23]
	v_lshl_add_u64 v[50:51], v[76:77], 0, v[14:15]
	v_lshl_add_u64 v[46:47], v[76:77], 0, v[20:21]
	v_lshl_add_u64 v[48:49], v[76:77], 0, v[12:13]
	global_load_dwordx4 v[30:33], v[38:39], off
	global_load_dwordx4 v[10:13], v[40:41], off
	global_load_dwordx4 v[26:29], v[44:45], off
	global_load_dwordx4 v[14:17], v[46:47], off
	global_load_dwordx4 v[34:37], v[48:49], off
	global_load_dwordx4 v[18:21], v[22:23], off
	v_lshl_add_u64 v[44:45], v[76:77], 0, v[24:25]
	global_load_dwordx4 v[38:41], v[50:51], off
	global_load_dwordx4 v[22:25], v[44:45], off
	ds_read2_b32 v[52:53], v114 offset0:40 offset1:44
	s_waitcnt lgkmcnt(1)
	v_ashrrev_i32_e32 v45, 31, v42
	v_mov_b32_e32 v44, v42
	v_lshlrev_b64 v[44:45], 8, v[44:45]
	v_lshl_add_u64 v[50:51], v[76:77], 0, v[44:45]
	v_ashrrev_i32_e32 v45, 31, v43
	v_mov_b32_e32 v44, v43
	v_lshlrev_b64 v[42:43], 8, v[44:45]
	v_lshl_add_u64 v[54:55], v[76:77], 0, v[42:43]
	global_load_dwordx4 v[46:49], v[50:51], off
	global_load_dwordx4 v[42:45], v[54:55], off
	s_waitcnt lgkmcnt(0)
	v_ashrrev_i32_e32 v51, 31, v52
	v_mov_b32_e32 v50, v52
	ds_read2_b32 v[60:61], v114 offset0:48 offset1:52
	v_lshlrev_b64 v[50:51], 8, v[50:51]
	v_lshl_add_u64 v[58:59], v[76:77], 0, v[50:51]
	v_ashrrev_i32_e32 v51, 31, v53
	v_mov_b32_e32 v50, v53
	v_lshlrev_b64 v[50:51], 8, v[50:51]
	v_lshl_add_u64 v[62:63], v[76:77], 0, v[50:51]
	global_load_dwordx4 v[54:57], v[58:59], off
	global_load_dwordx4 v[50:53], v[62:63], off
	ds_read2_b32 v[64:65], v114 offset0:56 offset1:60
	s_waitcnt lgkmcnt(1)
	v_ashrrev_i32_e32 v59, 31, v60
	v_mov_b32_e32 v58, v60
	v_lshlrev_b64 v[58:59], 8, v[58:59]
	v_lshl_add_u64 v[62:63], v[76:77], 0, v[58:59]
	v_ashrrev_i32_e32 v59, 31, v61
	v_mov_b32_e32 v58, v61
	v_lshlrev_b64 v[58:59], 8, v[58:59]
	v_lshl_add_u64 v[70:71], v[76:77], 0, v[58:59]
	global_load_dwordx4 v[66:69], v[62:63], off
	global_load_dwordx4 v[58:61], v[70:71], off
	s_waitcnt lgkmcnt(0)
	v_ashrrev_i32_e32 v63, 31, v64
	v_mov_b32_e32 v62, v64
	v_lshlrev_b64 v[62:63], 8, v[62:63]
	v_lshl_add_u64 v[80:81], v[76:77], 0, v[62:63]
	v_ashrrev_i32_e32 v63, 31, v65
	v_mov_b32_e32 v62, v65
	v_lshlrev_b64 v[62:63], 8, v[62:63]
	v_lshl_add_u64 v[82:83], v[76:77], 0, v[62:63]
	global_load_dwordx4 v[70:73], v[80:81], off
	global_load_dwordx4 v[62:65], v[82:83], off
	ds_read2_b32 v[80:81], v114 offset0:64 offset1:68
	ds_read2_b32 v[88:89], v114 offset0:72 offset1:76
	ds_read2_b32 v[82:83], v114 offset0:80 offset1:84
	ds_read2_b32 v[96:97], v114 offset0:88 offset1:92
	ds_read2_b32 v[100:101], v114 offset0:96 offset1:100
	ds_read2_b32 v[94:95], v114 offset0:104 offset1:108
	ds_read2_b32 v[92:93], v114 offset0:112 offset1:116
	ds_read2_b32 v[90:91], v114 offset0:120 offset1:124

.LBB0_2136:
	s_or_b64 exec, exec, s[2:3]
	s_mov_b64 s[2:3], s[0:1]
	s_waitcnt lgkmcnt(0)
	s_barrier
	v_readfirstlane_b32 s99, v0
	s_nop 3
	s_lshr_b32 s99, s99, 8
	s_cmp_eq_u32 s99, 0
	s_cbranch_scc1 .Lstag11_done
	s_sleep 56
.Lstag11_done:
	s_load_dwordx2 s[4:5], s[2:3], 0x90
	s_mov_b64 s[2:3], s[0:1]
	s_load_dwordx2 s[2:3], s[2:3], 0x90
	s_mov_b64 s[12:13], s[0:1]
	s_mov_b64 s[14:15], s[0:1]
	v_mov_b32_e32 v67, 0
	v_mov_b32_e32 v69, v67
	s_waitcnt lgkmcnt(0)
	s_add_u32 s8, s2, 0x40400000
	s_addc_u32 s9, s3, 0
	s_mov_b64 s[2:3], s[0:1]
	s_load_dwordx2 s[10:11], s[2:3], 0x90
	s_mov_b64 s[2:3], s[0:1]
	s_load_dwordx2 s[6:7], s[2:3], 0x90
	s_mov_b64 s[2:3], s[0:1]
	s_load_dwordx2 s[2:3], s[2:3], 0x90
	s_load_dwordx2 s[12:13], s[12:13], 0x90
	s_load_dwordx2 s[18:19], s[14:15], 0x90
	s_mov_b64 s[14:15], s[0:1]
	s_load_dwordx2 s[20:21], s[14:15], 0x18
	s_load_dwordx2 s[14:15], s[0:1], 0x88
	s_waitcnt lgkmcnt(0)
	s_add_u32 s16, s10, 0x20400000
	v_ashrrev_i32_e32 v4, 6, v0
	v_add_u32_e32 v138, s28, v4
	v_ashrrev_i32_e32 v139, 31, v138
	v_and_b32_e32 v1, 63, v0
	v_lshlrev_b64 v[2:3], 8, v[138:139]
	v_lshl_add_u64 v[2:3], s[8:9], 0, v[2:3]
	v_lshlrev_b32_e32 v68, 2, v1
	v_lshl_add_u64 v[2:3], v[2:3], 0, v[68:69]
	global_load_dword v16, v[2:3], off
	s_addc_u32 s17, s11, 0
	v_bfe_u32 v96, v0, 4, 2
	v_and_b32_e32 v97, 15, v0
	s_add_u32 s4, s4, s27
	v_lshlrev_b32_e32 v66, 4, v97
	v_lshlrev_b32_e32 v17, 2, v96
	v_and_b32_e32 v5, 31, v0
	s_addc_u32 s5, s5, 0
	v_or3_b32 v99, v17, s26, v66
	s_mov_b64 s[0:1], 0x12300000
	v_lshl_add_u32 v98, v4, 11, 0
	v_lshlrev_b32_e32 v70, 2, v5
	v_lshl_add_u64 v[4:5], s[4:5], 0, v[66:67]
	v_lshlrev_b32_e32 v66, 2, v99
	s_mov_b64 s[22:23], 0x24000
	s_mov_b32 s28, 0x24000
	v_lshl_add_u64 v[140:141], v[4:5], 0, s[0:1]
	v_lshl_add_u64 v[4:5], s[18:19], 0, v[66:67]
	v_lshl_add_u64 v[12:13], v[4:5], 0, s[22:23]
	v_add_co_u32_e32 v4, vcc, s28, v4
	s_mov_b64 s[24:25], 0x14000
	s_mov_b32 s29, 0x14000
	v_lshl_add_u64 v[10:11], s[20:21], 0, v[66:67]
	v_addc_co_u32_e32 v5, vcc, 0, v5, vcc
	v_lshl_add_u64 v[14:15], v[10:11], 0, s[24:25]
	v_add_co_u32_e32 v10, vcc, s29, v10
	s_mov_b32 s30, 0x10000
	v_lshlrev_b64 v[6:7], 7, v[138:139]
	v_addc_co_u32_e32 v11, vcc, 0, v11, vcc
	v_mov_b32_e32 v71, v67
	v_lshl_add_u64 v[6:7], s[16:17], 0, v[6:7]
	v_add_co_u32_e32 v2, vcc, s30, v2
	v_lshlrev_b64 v[8:9], 2, v[138:139]
	v_lshl_add_u64 v[6:7], v[6:7], 0, v[70:71]
	v_addc_co_u32_e32 v3, vcc, 0, v3, vcc
	v_lshl_add_u32 v143, v1, 3, v98
	v_lshl_add_u64 v[88:89], s[6:7], 0, v[8:9]
	global_load_dwordx4 v[72:75], v[4:5], off
	global_load_dwordx4 v[76:79], v[12:13], off offset:1024
	global_load_dwordx4 v[80:83], v[10:11], off
	global_load_dwordx4 v[84:87], v[14:15], off offset:1024
	global_load_dword v200, v[6:7], off
	global_load_dword v139, v[2:3], off
	s_mov_b32 s0, 0x20600000
	v_add_u32_e32 v201, v98, v17
	v_lshl_add_u64 v[90:91], s[2:3], 0, v[8:9]
	s_mov_b64 s[4:5], 0x20600000
	v_lshl_add_u64 v[160:161], s[14:15], 0, v[66:67]
	v_lshlrev_b32_e32 v66, 1, v99
	v_lshl_add_u64 v[144:145], v[88:89], 0, s[4:5]
	s_mov_b64 s[4:5], 0x20700000
	v_lshl_add_u64 v[66:67], s[12:13], 0, v[66:67]
	s_mov_b64 s[12:13], 0x34400000
	s_mov_b32 s11, 0
	v_lshl_add_u64 v[146:147], v[90:91], 0, s[4:5]
	v_add_u32_e32 v203, 0x200, v138
	v_lshl_add_u64 v[156:157], s[8:9], 0, v[68:69]
	v_cmp_gt_u32_e64 s[8:9], 32, v1
	v_lshl_add_u64 v[158:159], s[16:17], 0, v[70:71]
	v_lshl_add_u64 v[162:163], v[66:67], 0, s[12:13]
	v_add_u32_e32 v204, v98, v96
	v_add_u32_e32 v206, v98, v68
	s_mov_b32 s10, 0
	s_waitcnt vmcnt(6)
	v_and_b32_e32 v2, 0xffff, v16
	v_lshrrev_b32_e32 v3, 16, v16
	ds_write_b64 v143, v[2:3]
	v_add_co_u32_e32 v2, vcc, s0, v88
	s_mov_b32 s0, 0x20700000
	s_nop 0
	v_addc_co_u32_e32 v3, vcc, 0, v89, vcc
	global_load_dword v142, v[2:3], off
	ds_read2_b32 v[2:3], v201 offset1:4
	v_add_co_u32_e32 v4, vcc, s0, v90
	ds_read2_b32 v[10:11], v201 offset0:8 offset1:12
	s_nop 0
	v_addc_co_u32_e32 v5, vcc, 0, v91, vcc
	global_load_dword v202, v[4:5], off
	s_waitcnt lgkmcnt(1)
	v_ashrrev_i32_e32 v5, 31, v2
	v_mov_b32_e32 v4, v2
	v_lshlrev_b64 v[4:5], 8, v[4:5]
	v_lshl_add_u64 v[12:13], v[140:141], 0, v[4:5]
	v_ashrrev_i32_e32 v5, 31, v3
	v_mov_b32_e32 v4, v3
	v_lshlrev_b64 v[2:3], 8, v[4:5]
	v_lshl_add_u64 v[14:15], v[140:141], 0, v[2:3]
	global_load_dwordx4 v[6:9], v[12:13], off
	global_load_dwordx4 v[2:5], v[14:15], off
	s_waitcnt lgkmcnt(0)
	v_ashrrev_i32_e32 v13, 31, v10
	v_mov_b32_e32 v12, v10
	ds_read2_b32 v[20:21], v201 offset0:16 offset1:20
	v_lshlrev_b64 v[12:13], 8, v[12:13]
	v_lshl_add_u64 v[18:19], v[140:141], 0, v[12:13]
	v_ashrrev_i32_e32 v13, 31, v11
	v_mov_b32_e32 v12, v11
	v_lshlrev_b64 v[10:11], 8, v[12:13]
	v_lshl_add_u64 v[22:23], v[140:141], 0, v[10:11]
	global_load_dwordx4 v[14:17], v[18:19], off
	global_load_dwordx4 v[10:13], v[22:23], off
	ds_read2_b32 v[28:29], v201 offset0:24 offset1:28
	s_waitcnt lgkmcnt(1)
	v_ashrrev_i32_e32 v19, 31, v20
	v_mov_b32_e32 v18, v20
	v_lshlrev_b64 v[18:19], 8, v[18:19]
	v_lshl_add_u64 v[26:27], v[140:141], 0, v[18:19]
	v_ashrrev_i32_e32 v19, 31, v21
	v_mov_b32_e32 v18, v21
	v_lshlrev_b64 v[18:19], 8, v[18:19]
	v_lshl_add_u64 v[30:31], v[140:141], 0, v[18:19]
	global_load_dwordx4 v[22:25], v[26:27], off
	global_load_dwordx4 v[18:21], v[30:31], off
	s_waitcnt lgkmcnt(0)
	v_ashrrev_i32_e32 v27, 31, v28
	v_mov_b32_e32 v26, v28
	ds_read2_b32 v[36:37], v201 offset0:32 offset1:36
	v_lshlrev_b64 v[26:27], 8, v[26:27]
	v_lshl_add_u64 v[34:35], v[140:141], 0, v[26:27]
	v_ashrrev_i32_e32 v27, 31, v29
	v_mov_b32_e32 v26, v29
	v_lshlrev_b64 v[26:27], 8, v[26:27]
	v_lshl_add_u64 v[38:39], v[140:141], 0, v[26:27]
	global_load_dwordx4 v[30:33], v[34:35], off
	global_load_dwordx4 v[26:29], v[38:39], off
	ds_read2_b32 v[44:45], v201 offset0:40 offset1:44
	s_waitcnt lgkmcnt(1)
	v_ashrrev_i32_e32 v35, 31, v36
	v_mov_b32_e32 v34, v36
	v_lshlrev_b64 v[34:35], 8, v[34:35]
	v_lshl_add_u64 v[42:43], v[140:141], 0, v[34:35]
	v_ashrrev_i32_e32 v35, 31, v37
	v_mov_b32_e32 v34, v37
	v_lshlrev_b64 v[34:35], 8, v[34:35]
	v_lshl_add_u64 v[46:47], v[140:141], 0, v[34:35]
	global_load_dwordx4 v[38:41], v[42:43], off
	global_load_dwordx4 v[34:37], v[46:47], off
	s_waitcnt lgkmcnt(0)
	v_ashrrev_i32_e32 v43, 31, v44
	v_mov_b32_e32 v42, v44
	ds_read2_b32 v[52:53], v201 offset0:48 offset1:52
	v_lshlrev_b64 v[42:43], 8, v[42:43]
	v_lshl_add_u64 v[50:51], v[140:141], 0, v[42:43]
	v_ashrrev_i32_e32 v43, 31, v45
	v_mov_b32_e32 v42, v45
	v_lshlrev_b64 v[42:43], 8, v[42:43]
	v_lshl_add_u64 v[54:55], v[140:141], 0, v[42:43]
	global_load_dwordx4 v[46:49], v[50:51], off
	global_load_dwordx4 v[42:45], v[54:55], off
	ds_read2_b32 v[60:61], v201 offset0:56 offset1:60
	s_waitcnt lgkmcnt(1)
	v_ashrrev_i32_e32 v51, 31, v52
	v_mov_b32_e32 v50, v52
	v_lshlrev_b64 v[50:51], 8, v[50:51]
	v_lshl_add_u64 v[58:59], v[140:141], 0, v[50:51]
	v_ashrrev_i32_e32 v51, 31, v53
	v_mov_b32_e32 v50, v53
	v_lshlrev_b64 v[50:51], 8, v[50:51]
	v_lshl_add_u64 v[62:63], v[140:141], 0, v[50:51]
	global_load_dwordx4 v[54:57], v[58:59], off
	global_load_dwordx4 v[50:53], v[62:63], off
	s_waitcnt lgkmcnt(0)
	v_ashrrev_i32_e32 v59, 31, v60
	v_mov_b32_e32 v58, v60
	v_lshlrev_b64 v[58:59], 8, v[58:59]
	v_lshl_add_u64 v[92:93], v[140:141], 0, v[58:59]
	v_ashrrev_i32_e32 v59, 31, v61
	v_mov_b32_e32 v58, v61
	v_lshlrev_b64 v[58:59], 8, v[58:59]
	v_lshl_add_u64 v[94:95], v[140:141], 0, v[58:59]
	global_load_dwordx4 v[62:65], v[92:93], off
	global_load_dwordx4 v[58:61], v[94:95], off
	ds_read2_b32 v[164:165], v201 offset0:64 offset1:68
	ds_read2_b32 v[186:187], v201 offset0:72 offset1:76
	ds_read2_b32 v[166:167], v201 offset0:80 offset1:84
	ds_read2_b32 v[168:169], v201 offset0:88 offset1:92
	ds_read2_b32 v[170:171], v201 offset0:96 offset1:100
	ds_read2_b32 v[172:173], v201 offset0:104 offset1:108
	ds_read2_b32 v[174:175], v201 offset0:112 offset1:116
	ds_read2_b32 v[176:177], v201 offset0:120 offset1:124
	v_bfe_u32 v92, v0, 2, 2
	v_lshlrev_b32_e32 v0, 3, v0
	v_cmp_gt_u32_e64 s[0:1], 4, v97
	v_cmp_eq_u32_e64 s[2:3], 2, v92
	s_waitcnt vmcnt(21)
	v_pk_add_f32 v[148:149], v[74:75], v[82:83]
	v_pk_add_f32 v[150:151], v[72:73], v[80:81]
	s_waitcnt vmcnt(20)
	v_pk_add_f32 v[152:153], v[78:79], v[86:87]
	v_pk_add_f32 v[154:155], v[76:77], v[84:85]
	v_cmp_eq_u32_e64 s[4:5], 1, v92
	v_cmp_eq_u32_e64 s[6:7], 3, v92
	v_and_b32_e32 v205, 24, v0
